# speedup vs baseline: 1.0178x; 1.0064x over previous
.LBB3_36:
	s_andn2_b64 vcc, exec, s[6:7]
	s_cbranch_vccnz .LBB3_86
	s_cmpk_gt_u32 s2, 0xff
	s_cbranch_scc1 .LBB3_86
	s_mov_b64 s[40:41], s[0:1]
	s_mov_b32 s44, s18
	s_mov_b32 s45, s19
	s_mov_b32 s46, 0
	s_mov_b32 s60, s2
	s_mov_b32 s61, 0
	s_mov_b32 s65, 0
	s_mov_b32 s73, 0
	v_readfirstlane_b32 s72, v0
	s_nop 3
	s_cmp_ge_u32 s72, 0x100
	s_cselect_b32 s79, 1, 0
	s_load_dwordx2 s[68:69], s[0:1], 0x0
	s_load_dwordx2 s[70:71], s[0:1], 0x38
	s_mov_b32 s49, 0
	s_mov_b32 s47, 0
	s_mov_b32 s48, 0
	s_movk_i32 s50, 0x63
	s_load_dwordx2 s[52:53], s[0:1], 0x30
	s_add_i32 s51, s19, 31
	s_lshr_b32 s51, s51, 5
	s_sub_i32 s51, s51, 0x200
	s_sub_i32 s55, s51, 1
	s_cmp_lt_u32 s55, 0x80
	s_cselect_b32 s51, s51, 0
	v_mov_b32_e32 v248, v0

.LBB3_62:
	s_sub_i32 s66, s14, s67
	s_cmp_gt_u32 s66, 3
	s_cbranch_scc1 .Lpf_done
	s_cmp_eq_u32 s66, 0
	s_cbranch_scc1 .Lpf_0
	s_cmp_eq_u32 s73, 0
	s_cbranch_scc1 .Lpf_done
	s_cmp_eq_u32 s66, 1
	s_cbranch_scc1 .Lpf_1
	s_cmp_eq_u32 s66, 2
	s_cbranch_scc1 .Lpf_2
	s_waitcnt vmcnt(0)

.LBB3_63:
	s_cmp_eq_u32 s14, s50
	s_cbranch_scc1 .Lgru_dump
	s_cmp_eq_u32 s79, 0
	s_cbranch_scc1 .LBB3_66
	s_and_b32 s21, s14, 1
	s_mulk_i32 s21, 0x1e00
	v_add_u32_e32 v231, s21, v211
	ds_read_b128 v[166:169], v231
	s_cmp_lt_u32 s14, 2
	s_cbranch_scc1 .Lgru_l1_mid
	v_exp_f32_e32 v0, v2
	v_exp_f32_e32 v2, v3
	v_exp_f32_e32 v3, v4
	v_exp_f32_e32 v4, v5
	v_exp_f32_e32 v5, v6
	v_exp_f32_e32 v6, v7
	v_exp_f32_e32 v7, v8
	v_exp_f32_e32 v8, v9
	v_exp_f32_e32 v9, v10
	v_exp_f32_e32 v10, v11
	v_exp_f32_e32 v11, v12
	v_exp_f32_e32 v12, v13
	v_exp_f32_e32 v13, v14
	v_add_f32_e32 v0, 1.0, v0
	v_exp_f32_e32 v14, v18
	v_exp_f32_e32 v18, v19
	v_exp_f32_e32 v19, v20
	v_exp_f32_e32 v20, v21
	v_exp_f32_e32 v21, v22
	v_exp_f32_e32 v22, v23
	v_exp_f32_e32 v23, v24
	v_exp_f32_e32 v24, v25
	v_exp_f32_e32 v25, v26
	v_exp_f32_e32 v26, v27
	v_exp_f32_e32 v27, v28
	v_exp_f32_e32 v28, v29
	v_exp_f32_e32 v29, v30
	v_add_f32_e32 v30, 1.0, v2
	v_add_f32_e32 v65, 1.0, v11
	v_rcp_f32_e32 v2, v0
	v_add_f32_e32 v79, 1.0, v12
	v_rcp_f32_e32 v12, v65
	v_add_f32_e32 v31, 1.0, v3
	v_rcp_f32_e32 v3, v30
	v_add_f32_e32 v47, 1.0, v6
	v_add_f32_e32 v80, 1.0, v13
	v_rcp_f32_e32 v13, v79
	v_add_f32_e32 v32, 1.0, v4
	v_add_f32_e32 v48, 1.0, v7
	v_rcp_f32_e32 v4, v31
	v_rcp_f32_e32 v7, v47
	v_fma_f32 v0, v2, v34, v66
	v_add_f32_e32 v81, 1.0, v14
	v_rcp_f32_e32 v14, v80
	v_fma_f32 v66, v12, v44, v76
	v_exp_f32_e32 v0, v0
	v_add_f32_e32 v33, 1.0, v5
	v_add_f32_e32 v49, 1.0, v8
	v_rcp_f32_e32 v5, v32
	v_rcp_f32_e32 v8, v48
	v_fma_f32 v31, v3, v35, v67
	v_exp_f32_e32 v66, v66
	v_fma_f32 v67, v13, v45, v77
	v_exp_f32_e32 v31, v31
	v_rcp_f32_e32 v6, v33
	v_fma_f32 v32, v4, v36, v68
	v_fma_f32 v48, v7, v39, v71
	v_exp_f32_e32 v67, v67
	v_fma_f32 v68, v14, v46, v78
	v_exp_f32_e32 v32, v32
	v_exp_f32_e32 v48, v48
	v_add_f32_e32 v0, 1.0, v0
	v_add_f32_e32 v63, 1.0, v9
	v_rcp_f32_e32 v9, v49
	v_fma_f32 v33, v5, v37, v69
	v_fma_f32 v49, v8, v40, v72
	v_exp_f32_e32 v68, v68
	v_add_f32_e32 v76, 1.0, v66
	v_rcp_f32_e32 v66, v0
	v_exp_f32_e32 v33, v33
	v_exp_f32_e32 v49, v49
	v_add_f32_e32 v31, 1.0, v31
	v_fma_f32 v47, v6, v38, v70
	v_add_f32_e32 v77, 1.0, v67
	v_rcp_f32_e32 v67, v31
	v_add_f32_e32 v219, 1.0, v18
	v_rcp_f32_e32 v18, v81
	v_exp_f32_e32 v47, v47
	v_add_f32_e32 v32, 1.0, v32
	v_add_f32_e32 v48, 1.0, v48
	v_add_f32_e32 v78, 1.0, v68
	v_rcp_f32_e32 v68, v32
	v_rcp_f32_e32 v71, v48
	v_fma_f32 v66, v66, -2.0, 1.0
	v_add_f32_e32 v220, 1.0, v19
	v_rcp_f32_e32 v19, v219
	v_add_f32_e32 v33, 1.0, v33
	v_add_f32_e32 v49, 1.0, v49
	v_add_f32_e32 v64, 1.0, v10
	v_sub_f32_e32 v0, v50, v66
	v_rcp_f32_e32 v10, v63
	v_rcp_f32_e32 v69, v33
	v_rcp_f32_e32 v72, v49
	v_fma_f32 v67, v67, -2.0, 1.0
	v_add_f32_e32 v221, 1.0, v20
	v_rcp_f32_e32 v20, v220
	v_add_f32_e32 v47, 1.0, v47
	v_fma_f32 v50, v18, v0, v66
	v_rcp_f32_e32 v11, v64
	v_sub_f32_e32 v0, v51, v67
	v_fma_f32 v63, v9, v41, v73
	v_rcp_f32_e32 v70, v47
	v_fma_f32 v68, v68, -2.0, 1.0
	v_add_f32_e32 v222, 1.0, v21
	v_rcp_f32_e32 v21, v221
	v_exp_f32_e32 v63, v63
	v_fma_f32 v51, v19, v0, v67
	v_fma_f32 v64, v10, v42, v74
	v_sub_f32_e32 v0, v52, v68
	v_fma_f32 v69, v69, -2.0, 1.0
	v_add_f32_e32 v223, 1.0, v22
	v_rcp_f32_e32 v22, v222
	v_exp_f32_e32 v64, v64
	v_fma_f32 v52, v20, v0, v68
	v_fma_f32 v65, v11, v43, v75
	v_sub_f32_e32 v0, v53, v69
	v_fma_f32 v70, v70, -2.0, 1.0
	v_add_f32_e32 v224, 1.0, v23
	v_rcp_f32_e32 v23, v223
	v_exp_f32_e32 v65, v65
	v_add_f32_e32 v63, 1.0, v63
	v_fma_f32 v53, v21, v0, v69
	v_rcp_f32_e32 v73, v63
	v_sub_f32_e32 v0, v54, v70
	v_fma_f32 v71, v71, -2.0, 1.0
	v_add_f32_e32 v225, 1.0, v24
	v_rcp_f32_e32 v24, v224
	v_add_f32_e32 v64, 1.0, v64
	v_fma_f32 v54, v22, v0, v70
	v_rcp_f32_e32 v74, v64
	v_sub_f32_e32 v0, v55, v71
	v_fma_f32 v72, v72, -2.0, 1.0
	v_add_f32_e32 v226, 1.0, v25
	v_rcp_f32_e32 v25, v225
	v_add_f32_e32 v65, 1.0, v65
	v_fma_f32 v55, v23, v0, v71
	v_rcp_f32_e32 v75, v65
	v_sub_f32_e32 v0, v56, v72
	v_fma_f32 v73, v73, -2.0, 1.0
	v_add_f32_e32 v227, 1.0, v26
	v_rcp_f32_e32 v26, v226
	v_fma_f32 v56, v24, v0, v72
	v_rcp_f32_e32 v76, v76
	v_sub_f32_e32 v0, v57, v73
	v_fma_f32 v74, v74, -2.0, 1.0
	v_add_f32_e32 v228, 1.0, v27
	v_rcp_f32_e32 v27, v227
	v_fma_f32 v57, v25, v0, v73
	v_rcp_f32_e32 v77, v77
	v_sub_f32_e32 v0, v58, v74
	v_fma_f32 v75, v75, -2.0, 1.0
	v_add_f32_e32 v229, 1.0, v28
	v_rcp_f32_e32 v28, v228
	v_fma_f32 v58, v26, v0, v74
	v_rcp_f32_e32 v78, v78
	v_sub_f32_e32 v0, v59, v75
	v_fma_f32 v76, v76, -2.0, 1.0
	v_add_f32_e32 v230, 1.0, v29
	v_rcp_f32_e32 v29, v229
	v_fma_f32 v59, v27, v0, v75
	v_rcp_f32_e32 v30, v230
	v_sub_f32_e32 v0, v60, v76
	v_fma_f32 v77, v77, -2.0, 1.0
	v_fma_f32 v60, v28, v0, v76
	v_fma_f32 v78, v78, -2.0, 1.0
	v_sub_f32_e32 v0, v61, v77
	s_nop 0
	v_fma_f32 v61, v29, v0, v77
	v_sub_f32_e32 v0, v62, v78
	s_nop 0
	v_fma_f32 v62, v30, v0, v78
	v_cvt_pk_f16_f32 v33, v52, v53
	v_cvt_f16_f32_e32 v0, v62
	v_cvt_pk_f16_f32 v32, v50, v51
	v_cvt_pk_f16_f32 v49, v56, v57
	v_cvt_pk_f16_f32 v48, v54, v55
	ds_write2_b64 v210, v[32:33], v[48:49] offset1:2
	v_cvt_pk_f16_f32 v33, v60, v61
	v_cvt_pk_f16_f32 v32, v58, v59
	v_perm_b32 v0, v208, v0, s15
	ds_write_b64 v210, v[32:33] offset:32
	ds_write_b64 v218, v[0:1]
.Lgru_l1_mid:
	s_waitcnt lgkmcnt(0)
	s_barrier
	s_sub_i32 s8, s14, 1
	s_cmp_gt_u32 s8, 24
	s_cbranch_scc1 .LBB3_62
	s_branch .Lgru_l1_mfma
.LBB3_66:
	s_and_b32 s20, s14, 1
	s_xor_b32 s19, s20, 1
	s_cmp_gt_u32 s14, 24
	s_mov_b64 s[8:9], -1
	s_cbranch_scc0 .LBB3_71
	s_cmp_eq_u32 s14, 26
	s_cselect_b64 s[8:9], -1, 0
	s_and_b64 s[12:13], s[2:3], s[8:9]
	s_and_saveexec_b64 s[8:9], s[12:13]
	s_cbranch_execz .LBB3_70
	global_load_dwordx4 v[2:5], v[196:197], off
	global_load_dwordx4 v[6:9], v[196:197], off offset:1024
	global_load_dwordx4 v[10:13], v[196:197], off offset:2048
	global_load_dwordx4 v[14:17], v[196:197], off offset:3072
	global_load_dwordx4 v[18:21], v[198:199], off
	global_load_dwordx4 v[22:25], v[200:201], off
	global_load_dwordx4 v[26:29], v[202:203], off

.LBB3_71:
	s_andn2_b64 vcc, exec, s[8:9]
	s_cbranch_vccnz .LBB3_73
	s_setprio 1
	ds_read_b128 v[64:67], v213
	s_mul_i32 s8, s20, 0x5600
	v_add_u32_e32 v0, s8, v212
	s_waitcnt vmcnt(6)
	ds_read2_b64 v[2:5], v0 offset1:1
	ds_read_b128 v[220:223], v213 offset:1024
	ds_read2_b64 v[34:37], v0 offset0:4 offset1:5
	s_waitcnt vmcnt(2)
	ds_read2_b64 v[18:21], v0 offset0:28 offset1:29
	ds_read2_b64 v[38:41], v0 offset0:32 offset1:33
	s_mul_i32 s8, s20, 0x1e00
	v_add_u32_e32 v63, s8, v211
	s_min_u32 s8, s14, 22
	s_waitcnt vmcnt(0) lgkmcnt(1)
	v_mfma_f32_32x32x16_f16 v[18:33], v[64:67], v[18:21], 0
	v_mfma_f32_32x32x16_f16 v[2:17], v[64:67], v[2:5], 0
	s_waitcnt lgkmcnt(0)
	v_mfma_f32_32x32x16_f16 v[18:33], v[220:223], v[38:41], v[18:33]
	v_mfma_f32_32x32x16_f16 v[2:17], v[220:223], v[34:37], v[2:17]
	ds_read_b128 v[34:37], v63
	ds_read_b128 v[68:71], v63 offset:32
	s_waitcnt lgkmcnt(1)
	v_mfma_f32_32x32x16_f16 v[18:33], v[130:133], v[34:37], v[18:33]
	v_mfma_f32_32x32x16_f16 v[2:17], v[82:85], v[34:37], v[2:17]
	v_mfma_f32_32x32x16_f16 v[34:49], v[138:141], v[34:37], 0
	s_waitcnt lgkmcnt(0)
	v_mfma_f32_32x32x16_f16 v[18:33], v[110:113], v[68:71], v[18:33]
	v_mfma_f32_32x32x16_f16 v[2:17], v[86:89], v[68:71], v[2:17]
	v_mfma_f32_32x32x16_f16 v[34:49], v[142:145], v[68:71], v[34:49]
	ds_read_b128 v[68:71], v63 offset:64
	ds_read_b128 v[72:75], v63 offset:96
	s_waitcnt lgkmcnt(1)
	v_mfma_f32_32x32x16_f16 v[18:33], v[114:117], v[68:71], v[18:33]
	v_mfma_f32_32x32x16_f16 v[2:17], v[90:93], v[68:71], v[2:17]
	v_mfma_f32_32x32x16_f16 v[34:49], v[146:149], v[68:71], v[34:49]
	s_waitcnt lgkmcnt(0)
	v_mfma_f32_32x32x16_f16 v[18:33], v[118:121], v[72:75], v[18:33]
	v_mfma_f32_32x32x16_f16 v[2:17], v[94:97], v[72:75], v[2:17]
	v_mfma_f32_32x32x16_f16 v[34:49], v[150:153], v[72:75], v[34:49]
	ds_read_b128 v[68:71], v63 offset:128
	ds_read_b128 v[72:75], v63 offset:160
	s_waitcnt lgkmcnt(1)
	v_mfma_f32_32x32x16_f16 v[18:33], v[122:125], v[68:71], v[18:33]
	s_waitcnt lgkmcnt(0)
	v_mfma_f32_32x32x16_f16 v[18:33], v[126:129], v[72:75], v[18:33]
	v_mfma_f32_32x32x16_f16 v[2:17], v[106:109], v[68:71], v[2:17]
	v_mfma_f32_32x32x16_f16 v[34:49], v[154:157], v[68:71], v[34:49]
	ds_read_b128 v[68:71], v63 offset:192
	v_lshl_add_u32 v63, s8, 2, v214
	ds_read_b32 v63, v63 offset:8
	s_mul_i32 s8, s19, 0x5600
	s_waitcnt lgkmcnt(1)
	v_mfma_f32_32x32x16_f16 v[18:33], v[134:137], v[68:71], v[18:33]
	v_mfma_f32_32x32x16_f16 v[2:17], v[98:101], v[72:75], v[2:17]
	s_nop 10
	v_mov_b64_e32 v[32:33], s[10:11]
	v_mfma_f32_32x32x16_f16 v[34:49], v[158:161], v[72:75], v[34:49]
	ds_read2_b64 v[72:75], v0 offset0:56 offset1:57
	ds_read2_b64 v[224:227], v0 offset0:60 offset1:61
	v_add_u32_e32 v0, s8, v206
	s_waitcnt lgkmcnt(2)
	v_mad_i64_i32 v[32:33], s[8:9], v63, s18, v[32:33]
	v_lshl_add_u32 v31, v192, 1, v0
	ds_write_b128 v31, v[178:181]
	v_lshl_add_u64 v[228:229], v[192:193], 1, v[32:33]
	ds_write_b128 v31, v[174:177] offset:128
	global_load_dwordx4 v[178:181], v[228:229], off
	global_load_dwordx4 v[174:177], v[228:229], off offset:128
	ds_write_b128 v31, v[170:173] offset:256
	ds_write_b128 v31, v[166:169] offset:384
	v_lshl_add_u32 v0, v190, 1, v0
	global_load_dwordx4 v[170:173], v[228:229], off offset:256
	global_load_dwordx4 v[166:169], v[228:229], off offset:384
	ds_write_b128 v31, v[186:189] offset:512
	ds_write_b128 v0, v[182:185]
	v_lshl_add_u64 v[32:33], v[190:191], 1, v[32:33]
	global_load_dwordx4 v[186:189], v[228:229], off offset:512
	global_load_dwordx4 v[182:185], v[32:33], off
	v_mfma_f32_32x32x16_f16 v[2:17], v[102:105], v[68:71], v[2:17]
	v_mfma_f32_32x32x16_f16 v[34:49], v[162:165], v[68:71], v[34:49]
	s_waitcnt lgkmcnt(7)
	v_mfma_f32_32x32x16_f16 v[66:81], v[64:67], v[72:75], 0
	s_waitcnt lgkmcnt(6)
	v_mfma_f32_32x32x16_f16 v[66:81], v[220:223], v[224:227], v[66:81]
	s_setprio 0
.LBB3_73:
	s_waitcnt lgkmcnt(0)
	s_barrier
	s_branch .Lgru_l0_gates
.Lgru_l1_mfma:
	s_setprio 1
	ds_read_b128 v[220:223], v215 offset:15360
	ds_read_b128 v[170:173], v231 offset:32
	ds_read_b128 v[174:177], v231 offset:64
	ds_read_b128 v[178:181], v231 offset:96
	ds_read_b128 v[182:185], v231 offset:128
	ds_read_b128 v[186:189], v231 offset:160
	ds_read_b128 v[196:199], v231 offset:192
	v_mfma_f32_32x32x16_f16 v[2:17], v[232:235], v[166:169], 0
	v_mfma_f32_32x32x16_f16 v[18:33], v[236:239], v[166:169], 0
	ds_read_b128 v[232:235], v215 offset:2048
	v_mfma_f32_32x32x16_f16 v[66:81], v[240:243], v[166:169], 0
	ds_read_b128 v[236:239], v215 offset:9216
	s_waitcnt lgkmcnt(7)
	v_mfma_f32_32x32x16_f16 v[2:17], v[244:247], v[170:173], v[2:17]
	ds_read_b128 v[240:243], v215 offset:16384
	v_mfma_f32_32x32x16_f16 v[18:33], v[200:203], v[170:173], v[18:33]
	ds_read_b128 v[244:247], v215 offset:3072
	ds_read_b128 v[166:169], v216
	v_mfma_f32_32x32x16_f16 v[66:81], v[220:223], v[170:173], v[66:81]
	ds_read_b128 v[200:203], v215 offset:10240
	s_waitcnt lgkmcnt(5)
	v_mfma_f32_32x32x16_f16 v[2:17], v[232:235], v[174:177], v[2:17]
	ds_read_b128 v[220:223], v215 offset:17408
	s_waitcnt lgkmcnt(5)
	v_mfma_f32_32x32x16_f16 v[18:33], v[236:239], v[174:177], v[18:33]
	ds_read_b128 v[232:235], v215 offset:4096
	ds_read_b128 v[170:173], v216 offset:32
	s_waitcnt lgkmcnt(6)
	v_mfma_f32_32x32x16_f16 v[66:81], v[240:243], v[174:177], v[66:81]
	ds_read_b128 v[236:239], v215 offset:11264
	s_waitcnt lgkmcnt(6)
	v_mfma_f32_32x32x16_f16 v[2:17], v[244:247], v[178:181], v[2:17]
	ds_read_b128 v[240:243], v215 offset:18432
	s_waitcnt lgkmcnt(5)
	v_mfma_f32_32x32x16_f16 v[18:33], v[200:203], v[178:181], v[18:33]
	ds_read_b128 v[244:247], v215 offset:5120
	ds_read_b128 v[174:177], v216 offset:64
	s_waitcnt lgkmcnt(6)
	v_mfma_f32_32x32x16_f16 v[66:81], v[220:223], v[178:181], v[66:81]
	ds_read_b128 v[200:203], v215 offset:12288
	s_waitcnt lgkmcnt(6)
	v_mfma_f32_32x32x16_f16 v[2:17], v[232:235], v[182:185], v[2:17]
	ds_read_b128 v[220:223], v215 offset:19456
	s_waitcnt lgkmcnt(5)
	v_mfma_f32_32x32x16_f16 v[18:33], v[236:239], v[182:185], v[18:33]
	ds_read_b128 v[232:235], v215 offset:6144
	ds_read_b128 v[178:181], v216 offset:96
	s_waitcnt lgkmcnt(6)
	v_mfma_f32_32x32x16_f16 v[66:81], v[240:243], v[182:185], v[66:81]
	ds_read_b128 v[236:239], v215 offset:13312
	s_waitcnt lgkmcnt(6)
	v_mfma_f32_32x32x16_f16 v[2:17], v[244:247], v[186:189], v[2:17]
	ds_read_b128 v[240:243], v215 offset:20480
	s_waitcnt lgkmcnt(5)
	v_mfma_f32_32x32x16_f16 v[18:33], v[200:203], v[186:189], v[18:33]
	ds_read_b128 v[182:185], v216 offset:128
	s_waitcnt lgkmcnt(5)
	v_mfma_f32_32x32x16_f16 v[66:81], v[220:223], v[186:189], v[66:81]
	s_waitcnt lgkmcnt(4)
	v_mfma_f32_32x32x16_f16 v[2:17], v[232:235], v[196:199], v[2:17]
	s_waitcnt lgkmcnt(2)
	v_mfma_f32_32x32x16_f16 v[18:33], v[236:239], v[196:199], v[18:33]
	ds_read_b128 v[186:189], v216 offset:160
	s_waitcnt lgkmcnt(2)
	v_mfma_f32_32x32x16_f16 v[66:81], v[240:243], v[196:199], v[66:81]
	v_mfma_f32_32x32x16_f16 v[2:17], v[82:85], v[166:169], v[2:17]
	v_mfma_f32_32x32x16_f16 v[18:33], v[130:133], v[166:169], v[18:33]
	ds_read_b128 v[196:199], v216 offset:192
	v_mfma_f32_32x32x16_f16 v[34:49], v[138:141], v[166:169], 0
	v_mfma_f32_32x32x16_f16 v[2:17], v[86:89], v[170:173], v[2:17]
	ds_read_b128 v[232:235], v215
	v_mfma_f32_32x32x16_f16 v[18:33], v[110:113], v[170:173], v[18:33]
	ds_read_b128 v[236:239], v215 offset:7168
	v_mfma_f32_32x32x16_f16 v[34:49], v[142:145], v[170:173], v[34:49]
	ds_read_b128 v[240:243], v215 offset:14336
	v_mfma_f32_32x32x16_f16 v[2:17], v[90:93], v[174:177], v[2:17]
	ds_read_b128 v[244:247], v215 offset:1024
	v_mfma_f32_32x32x16_f16 v[18:33], v[114:117], v[174:177], v[18:33]
	ds_read_b128 v[200:203], v215 offset:8192
	v_mfma_f32_32x32x16_f16 v[34:49], v[146:149], v[174:177], v[34:49]
	v_mfma_f32_32x32x16_f16 v[2:17], v[94:97], v[178:181], v[2:17]
	v_mfma_f32_32x32x16_f16 v[18:33], v[118:121], v[178:181], v[18:33]
	v_mfma_f32_32x32x16_f16 v[34:49], v[150:153], v[178:181], v[34:49]
	s_waitcnt lgkmcnt(7)
	v_mfma_f32_32x32x16_f16 v[2:17], v[106:109], v[182:185], v[2:17]
	v_mfma_f32_32x32x16_f16 v[18:33], v[122:125], v[182:185], v[18:33]
	v_mfma_f32_32x32x16_f16 v[34:49], v[154:157], v[182:185], v[34:49]
	s_waitcnt lgkmcnt(6)
	v_mfma_f32_32x32x16_f16 v[2:17], v[98:101], v[186:189], v[2:17]
	v_mfma_f32_32x32x16_f16 v[18:33], v[126:129], v[186:189], v[18:33]
	v_mfma_f32_32x32x16_f16 v[34:49], v[158:161], v[186:189], v[34:49]
	s_waitcnt lgkmcnt(5)
	v_mfma_f32_32x32x16_f16 v[2:17], v[102:105], v[196:199], v[2:17]
	v_mfma_f32_32x32x16_f16 v[18:33], v[134:137], v[196:199], v[18:33]
	v_mfma_f32_32x32x16_f16 v[34:49], v[162:165], v[196:199], v[34:49]
	s_setprio 0
.LBB3_80:
	s_branch .LBB3_62
.Lgru_l0_gates:
	s_cmp_gt_u32 s14, 24
	s_cbranch_scc1 .LBB3_62
	v_exp_f32_e32 v0, v2
	v_exp_f32_e32 v2, v3
	v_exp_f32_e32 v3, v4
	v_exp_f32_e32 v4, v5
	v_exp_f32_e32 v5, v6
	v_exp_f32_e32 v6, v7
	v_exp_f32_e32 v7, v8
	v_exp_f32_e32 v8, v9
	v_exp_f32_e32 v9, v10
	v_exp_f32_e32 v10, v11
	v_exp_f32_e32 v11, v12
	v_exp_f32_e32 v12, v13
	v_exp_f32_e32 v13, v14
	v_add_f32_e32 v0, 1.0, v0
	v_exp_f32_e32 v14, v18
	v_exp_f32_e32 v18, v19
	v_exp_f32_e32 v19, v20
	v_exp_f32_e32 v20, v21
	v_exp_f32_e32 v21, v22
	v_exp_f32_e32 v22, v23
	v_exp_f32_e32 v23, v24
	v_exp_f32_e32 v24, v25
	v_exp_f32_e32 v25, v26
	v_exp_f32_e32 v26, v27
	v_exp_f32_e32 v27, v28
	v_exp_f32_e32 v28, v29
	v_exp_f32_e32 v29, v30
	v_add_f32_e32 v30, 1.0, v2
	v_add_f32_e32 v65, 1.0, v11
	v_rcp_f32_e32 v2, v0
	v_add_f32_e32 v79, 1.0, v12
	v_rcp_f32_e32 v12, v65
	v_add_f32_e32 v31, 1.0, v3
	v_rcp_f32_e32 v3, v30
	v_add_f32_e32 v47, 1.0, v6
	v_add_f32_e32 v80, 1.0, v13
	v_rcp_f32_e32 v13, v79
	v_add_f32_e32 v32, 1.0, v4
	v_add_f32_e32 v48, 1.0, v7
	v_rcp_f32_e32 v4, v31
	v_rcp_f32_e32 v7, v47
	v_fma_f32 v0, v2, v34, v66
	v_add_f32_e32 v81, 1.0, v14
	v_rcp_f32_e32 v14, v80
	v_fma_f32 v66, v12, v44, v76
	v_exp_f32_e32 v0, v0
	v_add_f32_e32 v33, 1.0, v5
	v_add_f32_e32 v49, 1.0, v8
	v_rcp_f32_e32 v5, v32
	v_rcp_f32_e32 v8, v48
	v_fma_f32 v31, v3, v35, v67
	v_exp_f32_e32 v66, v66
	v_fma_f32 v67, v13, v45, v77
	v_exp_f32_e32 v31, v31
	v_rcp_f32_e32 v6, v33
	v_fma_f32 v32, v4, v36, v68
	v_fma_f32 v48, v7, v39, v71
	v_exp_f32_e32 v67, v67
	v_fmac_f32_e32 v78, v14, v46
	v_exp_f32_e32 v32, v32
	v_exp_f32_e32 v48, v48
	v_add_f32_e32 v0, 1.0, v0
	v_add_f32_e32 v63, 1.0, v9
	v_rcp_f32_e32 v9, v49
	v_fma_f32 v33, v5, v37, v69
	v_fma_f32 v49, v8, v40, v72
	v_exp_f32_e32 v68, v78
	v_add_f32_e32 v76, 1.0, v66
	v_rcp_f32_e32 v66, v0
	v_exp_f32_e32 v33, v33
	v_exp_f32_e32 v49, v49
	v_add_f32_e32 v31, 1.0, v31
	v_fma_f32 v47, v6, v38, v70
	v_add_f32_e32 v77, 1.0, v67
	v_rcp_f32_e32 v67, v31
	v_add_f32_e32 v219, 1.0, v18
	v_rcp_f32_e32 v18, v81
	v_exp_f32_e32 v47, v47
	v_add_f32_e32 v32, 1.0, v32
	v_add_f32_e32 v48, 1.0, v48
	v_add_f32_e32 v78, 1.0, v68
	v_rcp_f32_e32 v68, v32
	v_rcp_f32_e32 v71, v48
	v_fma_f32 v66, v66, -2.0, 1.0
	v_add_f32_e32 v220, 1.0, v19
	v_rcp_f32_e32 v19, v219
	v_add_f32_e32 v33, 1.0, v33
	v_add_f32_e32 v49, 1.0, v49
	v_add_f32_e32 v64, 1.0, v10
	v_sub_f32_e32 v0, v50, v66
	v_rcp_f32_e32 v10, v63
	v_rcp_f32_e32 v69, v33
	v_rcp_f32_e32 v72, v49
	v_fma_f32 v67, v67, -2.0, 1.0
	v_add_f32_e32 v221, 1.0, v20
	v_rcp_f32_e32 v20, v220
	v_add_f32_e32 v47, 1.0, v47
	v_fma_f32 v50, v18, v0, v66
	v_rcp_f32_e32 v11, v64
	v_sub_f32_e32 v0, v51, v67
	v_fma_f32 v63, v9, v41, v73
	v_rcp_f32_e32 v70, v47
	v_fma_f32 v68, v68, -2.0, 1.0
	v_add_f32_e32 v222, 1.0, v21
	v_rcp_f32_e32 v21, v221
	v_exp_f32_e32 v63, v63
	v_fma_f32 v51, v19, v0, v67
	v_fma_f32 v64, v10, v42, v74
	v_sub_f32_e32 v0, v52, v68
	v_fma_f32 v69, v69, -2.0, 1.0
	v_add_f32_e32 v223, 1.0, v22
	v_rcp_f32_e32 v22, v222
	v_exp_f32_e32 v64, v64
	v_fma_f32 v52, v20, v0, v68
	v_fma_f32 v65, v11, v43, v75
	v_sub_f32_e32 v0, v53, v69
	v_fma_f32 v70, v70, -2.0, 1.0
	v_add_f32_e32 v224, 1.0, v23
	v_rcp_f32_e32 v23, v223
	v_exp_f32_e32 v65, v65
	v_add_f32_e32 v63, 1.0, v63
	v_fma_f32 v53, v21, v0, v69
	v_rcp_f32_e32 v73, v63
	v_sub_f32_e32 v0, v54, v70
	v_fma_f32 v71, v71, -2.0, 1.0
	v_add_f32_e32 v225, 1.0, v24
	v_rcp_f32_e32 v24, v224
	v_add_f32_e32 v64, 1.0, v64
	v_fma_f32 v54, v22, v0, v70
	v_rcp_f32_e32 v74, v64
	v_sub_f32_e32 v0, v55, v71
	v_fma_f32 v72, v72, -2.0, 1.0
	v_add_f32_e32 v226, 1.0, v25
	v_rcp_f32_e32 v25, v225
	v_add_f32_e32 v65, 1.0, v65
	v_fma_f32 v55, v23, v0, v71
	v_rcp_f32_e32 v75, v65
	v_sub_f32_e32 v0, v56, v72
	v_fma_f32 v73, v73, -2.0, 1.0
	v_add_f32_e32 v227, 1.0, v26
	v_rcp_f32_e32 v26, v226
	v_fma_f32 v56, v24, v0, v72
	v_rcp_f32_e32 v76, v76
	v_sub_f32_e32 v0, v57, v73
	v_fma_f32 v74, v74, -2.0, 1.0
	v_add_f32_e32 v228, 1.0, v27
	v_rcp_f32_e32 v27, v227
	v_fma_f32 v57, v25, v0, v73
	v_rcp_f32_e32 v77, v77
	v_sub_f32_e32 v0, v58, v74
	v_fma_f32 v75, v75, -2.0, 1.0
	v_add_f32_e32 v229, 1.0, v28
	v_rcp_f32_e32 v28, v228
	v_fma_f32 v58, v26, v0, v74
	v_rcp_f32_e32 v78, v78
	v_sub_f32_e32 v0, v59, v75
	v_fma_f32 v76, v76, -2.0, 1.0
	v_add_f32_e32 v230, 1.0, v29
	v_rcp_f32_e32 v29, v229
	v_fma_f32 v59, v27, v0, v75
	v_rcp_f32_e32 v30, v230
	v_sub_f32_e32 v0, v60, v76
	v_fma_f32 v77, v77, -2.0, 1.0
	v_fma_f32 v60, v28, v0, v76
	v_fma_f32 v78, v78, -2.0, 1.0
	v_sub_f32_e32 v0, v61, v77
	s_mulk_i32 s19, 0x1e00
	v_fma_f32 v61, v29, v0, v77
	v_sub_f32_e32 v0, v62, v78
	s_nop 0
	v_fma_f32 v62, v30, v0, v78
	v_add_u32_e32 v31, s19, v217
	v_cvt_f16_f32_e32 v0, v62
	v_cvt_pk_f16_f32 v33, v52, v53
	v_cvt_pk_f16_f32 v32, v50, v51
	v_cvt_pk_f16_f32 v49, v56, v57
	v_cvt_pk_f16_f32 v48, v54, v55
	ds_write2_b64 v31, v[32:33], v[48:49] offset1:2
	v_cvt_pk_f16_f32 v33, v60, v61
	v_cvt_pk_f16_f32 v32, v58, v59
	ds_write_b64 v31, v[32:33] offset:32
	v_add_u32_e32 v31, 48, v31
	v_perm_b32 v0, v208, v0, s15
	v_cndmask_b32_e64 v31, v209, v31, s[4:5]
	ds_write_b64 v31, v[0:1]
	s_branch .LBB3_62
